# SB tile trim: drop 32 canonicalising v_max, hoist tri/ones suffix-sum operands per unit, one V base + DS offsets, no shifted C re-broadcast
# baseline (speedup 1.0000x reference)
.LBB0_515:
	v_ashrrev_i32_e32 v118, 3, v119
	v_lshlrev_b32_e32 v7, 1, v119
	v_lshlrev_b32_e32 v9, 6, v118
	v_and_b32_e32 v7, 32, v7
	v_and_b32_e32 v9, 0xffffff00, v9
	v_and_b32_e32 v4, 0xc0, v4
	v_lshlrev_b32_e32 v8, 3, v119
	v_or3_b32 v4, v9, v4, v7
	v_lshlrev_b32_e32 v5, 4, v163
	v_lshlrev_b32_e32 v6, 2, v3
	v_and_b32_e32 v8, 24, v8
	v_add_u32_e32 v167, 0x2000, v4
	v_add_u32_e32 v167, v167, v8
	v_add_u32_e32 v4, s28, v163
	v_mov_b32_e32 v16, v2
	v_mov_b32_e32 v17, v2
	v_sub_u32_e32 v166, v163, v6
	v_sub_u32_e32 v184, v4, v6
	v_lshl_or_b32 v185, v3, 10, v5
	v_cmp_gt_i32_e32 vcc, 0, v166
	s_nop 1
	v_cndmask_b32_e32 v5, 0, v162, vcc
	v_cmp_lt_i32_e32 vcc, 0, v166
	s_nop 1
	v_cndmask_b32_e64 v6, 1.0, 0, vcc
	v_or_b32_e32 v172, v5, v6
	v_cmp_gt_i32_e32 vcc, 2, v166
	s_nop 1
	v_cndmask_b32_e32 v5, 0, v162, vcc
	v_cmp_lt_i32_e32 vcc, 2, v166
	s_nop 1
	v_cndmask_b32_e64 v6, 1.0, 0, vcc
	v_or_b32_e32 v173, v5, v6
	v_cmp_gt_i32_e32 vcc, 8, v166
	s_nop 1
	v_cndmask_b32_e32 v5, 0, v162, vcc
	v_cmp_lt_i32_e32 vcc, 8, v166
	s_nop 1
	v_cndmask_b32_e64 v6, 1.0, 0, vcc
	v_or_b32_e32 v174, v5, v6
	v_cmp_gt_i32_e32 vcc, 10, v166
	s_nop 1
	v_cndmask_b32_e32 v5, 0, v162, vcc
	v_cmp_lt_i32_e32 vcc, 10, v166
	s_nop 1
	v_cndmask_b32_e64 v6, 1.0, 0, vcc
	v_or_b32_e32 v175, v5, v6
	v_cmp_gt_i32_e32 vcc, 16, v166
	s_nop 1
	v_cndmask_b32_e32 v5, 0, v162, vcc
	v_cmp_lt_i32_e32 vcc, 16, v166
	s_nop 1
	v_cndmask_b32_e64 v6, 1.0, 0, vcc
	v_or_b32_e32 v176, v5, v6
	v_cmp_gt_i32_e32 vcc, 18, v166
	s_nop 1
	v_cndmask_b32_e32 v5, 0, v162, vcc
	v_cmp_lt_i32_e32 vcc, 18, v166
	s_nop 1
	v_cndmask_b32_e64 v6, 1.0, 0, vcc
	v_or_b32_e32 v177, v5, v6
	v_cmp_gt_i32_e32 vcc, 24, v166
	s_nop 1
	v_cndmask_b32_e32 v5, 0, v162, vcc
	v_cmp_lt_i32_e32 vcc, 24, v166
	s_nop 1
	v_cndmask_b32_e64 v6, 1.0, 0, vcc
	v_or_b32_e32 v178, v5, v6
	v_cmp_gt_i32_e32 vcc, 26, v166
	s_nop 1
	v_cndmask_b32_e32 v5, 0, v162, vcc
	v_cmp_lt_i32_e32 vcc, 26, v166
	s_nop 1
	v_cndmask_b32_e64 v6, 1.0, 0, vcc
	v_or_b32_e32 v179, v5, v6
	v_mov_b32_e32 v180, 0x3f803f80
	v_mov_b32_e32 v181, 0x3f803f80
	v_mov_b32_e32 v182, 0x3f803f80
	v_mov_b32_e32 v183, 0x3f803f80
	v_mov_b32_e32 v3, v2
	v_mov_b32_e32 v4, v2
	v_mov_b32_e32 v5, v2
	v_mov_b32_e32 v6, v2
	v_mov_b32_e32 v7, v2
	v_mov_b32_e32 v8, v2
	v_mov_b32_e32 v9, v2
	v_mov_b32_e32 v10, v2
	v_mov_b32_e32 v11, v2
	v_mov_b32_e32 v12, v2
	v_mov_b32_e32 v13, v2
	v_mov_b32_e32 v14, v2
	v_mov_b32_e32 v15, v2
	v_mov_b64_e32 v[34:35], v[16:17]
	v_and_b32_e32 v164, 7, v119
	s_lshl_b32 s4, s4, 8
	v_mov_b64_e32 v[32:33], v[14:15]
	v_mov_b64_e32 v[30:31], v[12:13]
	v_mov_b64_e32 v[28:29], v[10:11]
	v_mov_b64_e32 v[26:27], v[8:9]
	v_mov_b64_e32 v[24:25], v[6:7]
	v_mov_b64_e32 v[22:23], v[4:5]
	v_mov_b64_e32 v[20:21], v[2:3]
	v_mov_b64_e32 v[18:19], v[16:17]
	s_add_i32 s16, s3, -2
	s_or_b32 s37, s34, 30
	v_lshl_add_u32 v165, v164, 2, s31
	s_mov_b32 s38, 4
	s_mov_b32 s39, 0
	v_cmp_eq_u32_e64 s[2:3], 0, v119
	s_sub_i32 s40, s5, 31
	s_sub_i32 s41, 0x7c0, s4
	s_sub_i32 s42, 31, s5
	s_mov_b64 s[4:5], 0
	v_mov_b32_e32 v36, 0
	s_mov_b32 s43, 5
	s_mov_b32 s44, 0
	s_mov_b32 s45, 0
	s_mov_b32 s46, 0
	v_mov_b64_e32 v[16:17], v[14:15]
	v_mov_b64_e32 v[14:15], v[12:13]
	v_mov_b64_e32 v[12:13], v[10:11]
	v_mov_b64_e32 v[10:11], v[8:9]
	v_mov_b64_e32 v[8:9], v[6:7]
	v_mov_b64_e32 v[6:7], v[4:5]
	v_mov_b64_e32 v[4:5], v[2:3]
	s_branch .LBB0_518

.LBB0_538:
	s_xor_b64 s[4:5], s[4:5], -1
	s_andn2_b64 vcc, exec, s[4:5]
	s_mov_b64 s[4:5], -1
	s_cbranch_vccnz .LBB0_545
	s_cmp_gt_i32 s41, s37
	s_mov_b64 s[4:5], 0
	s_cbranch_scc1 .LBB0_545
	s_mul_hi_u32 s4, s46, 0xaaaaaaab
	s_lshr_b32 s17, s4, 2
	s_mul_i32 s17, s17, 0x18000
	v_subrev_u32_e32 v3, s17, v185
	s_add_i32 s4, s44, 0
	v_add_u32_e32 v3, s4, v3
	ds_read_b128 v[38:41], v3
	ds_read_b128 v[42:45], v3 offset:512
	ds_read_b128 v[86:89], v3 offset:2048
	ds_read_b128 v[90:93], v3 offset:2560
	s_add_i32 s18, s41, 63
	s_waitcnt lgkmcnt(3)
	v_mfma_f32_32x32x16_bf16 v[54:69], v[38:41], v[82:85], 0
	s_mov_b64 s[4:5], -1
	s_cmp_lt_i32 s18, s34
	s_waitcnt lgkmcnt(2)
	v_mfma_f32_32x32x16_bf16 v[38:53], v[42:45], v[82:85], 0
	s_waitcnt lgkmcnt(1)
	v_mfma_f32_32x32x16_bf16 v[54:69], v[86:89], v[78:81], v[54:69]
	s_waitcnt lgkmcnt(0)
	v_mfma_f32_32x32x16_bf16 v[38:53], v[90:93], v[78:81], v[38:53]
	ds_read_b128 v[86:89], v3 offset:4096
	ds_read_b128 v[90:93], v3 offset:4608
	s_waitcnt lgkmcnt(1)
	v_mfma_f32_32x32x16_bf16 v[54:69], v[86:89], v[74:77], v[54:69]
	s_waitcnt lgkmcnt(0)
	v_mfma_f32_32x32x16_bf16 v[38:53], v[90:93], v[74:77], v[38:53]
	ds_read_b128 v[86:89], v3 offset:6144
	ds_read_b128 v[90:93], v3 offset:6656
	s_waitcnt lgkmcnt(1)
	v_mfma_f32_32x32x16_bf16 v[54:69], v[86:89], v[70:73], v[54:69]
	s_waitcnt lgkmcnt(0)
	v_mfma_f32_32x32x16_bf16 v[38:53], v[90:93], v[70:73], v[38:53]
	s_nop 9
	v_exp_f32_e64 v247, -|v54|
	v_exp_f32_e64 v246, -|v55|
	v_exp_f32_e64 v239, -|v56|
	v_exp_f32_e64 v238, -|v57|
	v_exp_f32_e64 v231, -|v58|
	v_exp_f32_e64 v230, -|v59|
	v_exp_f32_e64 v223, -|v60|
	v_exp_f32_e64 v243, -|v38|
	v_exp_f32_e64 v242, -|v39|
	v_exp_f32_e64 v235, -|v40|
	v_exp_f32_e64 v234, -|v41|
	v_exp_f32_e64 v227, -|v42|
	v_exp_f32_e64 v226, -|v43|
	v_exp_f32_e64 v222, -|v61|
	v_exp_f32_e64 v219, -|v44|
	v_exp_f32_e64 v218, -|v45|
	v_exp_f32_e64 v215, -|v62|
	v_exp_f32_e64 v213, -|v63|
	v_exp_f32_e64 v211, -|v46|
	v_exp_f32_e64 v210, -|v47|
	v_exp_f32_e64 v207, -|v64|
	v_exp_f32_e64 v206, -|v65|
	v_exp_f32_e64 v203, -|v48|
	v_exp_f32_e64 v202, -|v49|
	v_exp_f32_e64 v199, -|v66|
	v_exp_f32_e64 v198, -|v67|
	v_exp_f32_e64 v195, -|v50|
	v_exp_f32_e64 v194, -|v51|
	v_exp_f32_e64 v190, -|v68|
	v_exp_f32_e64 v189, -|v69|
	v_exp_f32_e64 v187, -|v52|
	v_exp_f32_e64 v186, -|v53|
	s_cbranch_scc1 .LBB0_542
	v_add_f32_e32 v86, 1.0, v247
	v_add_f32_e32 v87, 1.0, v246
	v_log_f32_e32 v86, v86
	v_log_f32_e32 v87, v87
	v_max_f32_e32 v88, 0, v54
	v_max_f32_e32 v89, 0, v55
	v_cmp_lt_i32_e32 vcc, 0, v184
	v_pk_add_f32 v[86:87], v[88:89], v[86:87]
	v_cmp_lt_i32_e64 s[4:5], 1, v184
	v_pk_add_f32 v[88:89], v[54:55], v[86:87] neg_lo:[0,1] neg_hi:[0,1]
	v_cndmask_b32_e32 v86, 0, v86, vcc
	v_cndmask_b32_e64 v87, 0, v87, s[4:5]
	v_and_b32_e32 v91, 0xffff0000, v87
	v_and_b32_e32 v90, 0xffff0000, v86
	v_cndmask_b32_e32 v124, v161, v88, vcc
	v_cndmask_b32_e64 v125, v161, v89, s[4:5]
	v_pk_add_f32 v[88:89], v[86:87], 0 op_sel_hi:[1,0]
	v_or_b32_sdwa v98, v91, v86 dst_sel:DWORD dst_unused:UNUSED_PAD src0_sel:DWORD src1_sel:WORD_1
	v_pk_add_f32 v[86:87], v[86:87], v[90:91] neg_lo:[0,1] neg_hi:[0,1]
	v_add_f32_e32 v90, 1.0, v243
	v_add_f32_e32 v91, 1.0, v242
	v_log_f32_e32 v90, v90
	v_log_f32_e32 v91, v91
	v_cvt_pk_bf16_f32 v94, v86, v87
	v_max_f32_e32 v86, 0, v38
	v_max_f32_e32 v87, 0, v39
	v_pk_add_f32 v[86:87], v[86:87], v[90:91]
	v_cmp_lt_i32_e32 vcc, 32, v184
	v_pk_add_f32 v[90:91], v[38:39], v[86:87] neg_lo:[0,1] neg_hi:[0,1]
	v_cmp_lt_i32_e64 s[4:5], 33, v184
	v_cndmask_b32_e32 v126, v161, v90, vcc
	v_cndmask_b32_e32 v90, 0, v86, vcc
	v_cndmask_b32_e64 v127, v161, v91, s[4:5]
	v_cndmask_b32_e64 v91, 0, v87, s[4:5]
	v_and_b32_e32 v93, 0xffff0000, v91
	v_and_b32_e32 v92, 0xffff0000, v90
	v_add_f32_e32 v87, 1.0, v239
	v_pk_add_f32 v[88:89], v[90:91], v[88:89]
	v_or_b32_sdwa v86, v93, v90 dst_sel:DWORD dst_unused:UNUSED_PAD src0_sel:DWORD src1_sel:WORD_1
	v_pk_add_f32 v[90:91], v[90:91], v[92:93] neg_lo:[0,1] neg_hi:[0,1]
	v_log_f32_e32 v92, v87
	v_add_f32_e32 v87, 1.0, v238
	v_log_f32_e32 v93, v87
	v_max_f32_e32 v96, 0, v56
	v_max_f32_e32 v97, 0, v57
	v_cmp_lt_i32_e32 vcc, 2, v184
	v_pk_add_f32 v[92:93], v[96:97], v[92:93]
	v_cmp_lt_i32_e64 s[4:5], 3, v184
	v_pk_add_f32 v[96:97], v[56:57], v[92:93] neg_lo:[0,1] neg_hi:[0,1]
	v_cndmask_b32_e32 v92, 0, v92, vcc
	v_cndmask_b32_e64 v93, 0, v93, s[4:5]
	v_cndmask_b32_e32 v128, v161, v96, vcc
	v_cndmask_b32_e64 v129, v161, v97, s[4:5]
	v_and_b32_e32 v97, 0xffff0000, v93
	v_and_b32_e32 v96, 0xffff0000, v92
	v_add_f32_e32 v87, 1.0, v235
	v_pk_add_f32 v[88:89], v[92:93], v[88:89]
	v_or_b32_sdwa v99, v97, v92 dst_sel:DWORD dst_unused:UNUSED_PAD src0_sel:DWORD src1_sel:WORD_1
	v_pk_add_f32 v[92:93], v[92:93], v[96:97] neg_lo:[0,1] neg_hi:[0,1]
	v_log_f32_e32 v96, v87
	v_add_f32_e32 v87, 1.0, v234
	v_log_f32_e32 v97, v87
	v_cvt_pk_bf16_f32 v95, v92, v93
	v_max_f32_e32 v92, 0, v40
	v_max_f32_e32 v93, 0, v41
	v_pk_add_f32 v[92:93], v[92:93], v[96:97]
	v_cmp_lt_i32_e32 vcc, 34, v184
	v_cmp_lt_i32_e64 s[4:5], 35, v184
	v_pk_add_f32 v[96:97], v[40:41], v[92:93] neg_lo:[0,1] neg_hi:[0,1]
	v_cndmask_b32_e32 v92, 0, v92, vcc
	v_cndmask_b32_e64 v93, 0, v93, s[4:5]
	v_cvt_pk_bf16_f32 v90, v90, v91
	v_cndmask_b32_e32 v130, v161, v96, vcc
	v_cndmask_b32_e64 v131, v161, v97, s[4:5]
	v_and_b32_e32 v97, 0xffff0000, v93
	v_and_b32_e32 v96, 0xffff0000, v92
	v_add_f32_e32 v91, 1.0, v231
	v_pk_add_f32 v[88:89], v[92:93], v[88:89]
	v_or_b32_sdwa v87, v97, v92 dst_sel:DWORD dst_unused:UNUSED_PAD src0_sel:DWORD src1_sel:WORD_1
	v_pk_add_f32 v[92:93], v[92:93], v[96:97] neg_lo:[0,1] neg_hi:[0,1]
	v_log_f32_e32 v96, v91
	v_add_f32_e32 v91, 1.0, v230
	v_log_f32_e32 v97, v91
	v_cvt_pk_bf16_f32 v91, v92, v93
	v_max_f32_e32 v92, 0, v58
	v_max_f32_e32 v93, 0, v59
	v_pk_add_f32 v[92:93], v[92:93], v[96:97]
	v_cmp_lt_i32_e32 vcc, 8, v184
	v_cmp_lt_i32_e64 s[4:5], 9, v184
	v_pk_add_f32 v[96:97], v[58:59], v[92:93] neg_lo:[0,1] neg_hi:[0,1]
	v_cndmask_b32_e32 v92, 0, v92, vcc
	v_cndmask_b32_e64 v93, 0, v93, s[4:5]
	v_cndmask_b32_e32 v132, v161, v96, vcc
	v_cndmask_b32_e64 v133, v161, v97, s[4:5]
	v_and_b32_e32 v97, 0xffff0000, v93
	v_and_b32_e32 v96, 0xffff0000, v92
	v_pk_add_f32 v[88:89], v[92:93], v[88:89]
	v_or_b32_sdwa v100, v97, v92 dst_sel:DWORD dst_unused:UNUSED_PAD src0_sel:DWORD src1_sel:WORD_1
	v_pk_add_f32 v[92:93], v[92:93], v[96:97] neg_lo:[0,1] neg_hi:[0,1]
	v_add_f32_e32 v96, 1.0, v227
	v_log_f32_e32 v102, v96
	v_add_f32_e32 v96, 1.0, v226
	v_log_f32_e32 v103, v96
	v_cvt_pk_bf16_f32 v96, v92, v93
	v_max_f32_e32 v92, 0, v42
	v_max_f32_e32 v93, 0, v43
	v_pk_add_f32 v[92:93], v[92:93], v[102:103]
	v_cmp_lt_i32_e32 vcc, 40, v184
	v_cmp_lt_i32_e64 s[4:5], 41, v184
	v_pk_add_f32 v[102:103], v[42:43], v[92:93] neg_lo:[0,1] neg_hi:[0,1]
	v_cndmask_b32_e32 v92, 0, v92, vcc
	v_cndmask_b32_e64 v93, 0, v93, s[4:5]
	v_cndmask_b32_e32 v134, v161, v102, vcc
	v_cndmask_b32_e64 v135, v161, v103, s[4:5]
	v_pk_add_f32 v[102:103], v[92:93], v[88:89]
	v_and_b32_e32 v105, 0xffff0000, v93
	v_and_b32_e32 v104, 0xffff0000, v92
	v_add_f32_e32 v89, 1.0, v223
	v_or_b32_sdwa v88, v105, v92 dst_sel:DWORD dst_unused:UNUSED_PAD src0_sel:DWORD src1_sel:WORD_1
	v_pk_add_f32 v[92:93], v[92:93], v[104:105] neg_lo:[0,1] neg_hi:[0,1]
	v_log_f32_e32 v104, v89
	v_add_f32_e32 v89, 1.0, v222
	v_log_f32_e32 v105, v89
	v_max_f32_e32 v106, 0, v60
	v_max_f32_e32 v107, 0, v61
	v_cmp_lt_i32_e32 vcc, 10, v184
	v_pk_add_f32 v[104:105], v[106:107], v[104:105]
	v_cmp_lt_i32_e64 s[4:5], 11, v184
	v_pk_add_f32 v[106:107], v[60:61], v[104:105] neg_lo:[0,1] neg_hi:[0,1]
	v_cndmask_b32_e32 v104, 0, v104, vcc
	v_cndmask_b32_e64 v105, 0, v105, s[4:5]
	v_cndmask_b32_e32 v136, v161, v106, vcc
	v_cndmask_b32_e64 v137, v161, v107, s[4:5]
	v_and_b32_e32 v107, 0xffff0000, v105
	v_and_b32_e32 v106, 0xffff0000, v104
	v_add_f32_e32 v89, 1.0, v219
	v_pk_add_f32 v[102:103], v[104:105], v[102:103]
	v_or_b32_sdwa v101, v107, v104 dst_sel:DWORD dst_unused:UNUSED_PAD src0_sel:DWORD src1_sel:WORD_1
	v_pk_add_f32 v[104:105], v[104:105], v[106:107] neg_lo:[0,1] neg_hi:[0,1]
	v_log_f32_e32 v106, v89
	v_add_f32_e32 v89, 1.0, v218
	v_log_f32_e32 v107, v89
	v_cvt_pk_bf16_f32 v97, v104, v105
	v_max_f32_e32 v104, 0, v44
	v_max_f32_e32 v105, 0, v45
	v_pk_add_f32 v[104:105], v[104:105], v[106:107]
	v_cmp_lt_i32_e32 vcc, 42, v184
	v_cmp_lt_i32_e64 s[4:5], 43, v184
	v_pk_add_f32 v[106:107], v[44:45], v[104:105] neg_lo:[0,1] neg_hi:[0,1]
	v_cndmask_b32_e32 v104, 0, v104, vcc
	v_cndmask_b32_e64 v105, 0, v105, s[4:5]
	v_cvt_pk_bf16_f32 v92, v92, v93
	v_cndmask_b32_e32 v138, v161, v106, vcc
	v_cndmask_b32_e64 v139, v161, v107, s[4:5]
	v_and_b32_e32 v107, 0xffff0000, v105
	v_and_b32_e32 v106, 0xffff0000, v104
	v_add_f32_e32 v93, 1.0, v215
	v_pk_add_f32 v[102:103], v[104:105], v[102:103]
	v_or_b32_sdwa v89, v107, v104 dst_sel:DWORD dst_unused:UNUSED_PAD src0_sel:DWORD src1_sel:WORD_1
	v_pk_add_f32 v[104:105], v[104:105], v[106:107] neg_lo:[0,1] neg_hi:[0,1]
	v_log_f32_e32 v106, v93
	v_add_f32_e32 v93, 1.0, v213
	v_log_f32_e32 v107, v93
	v_cvt_pk_bf16_f32 v93, v104, v105
	v_max_f32_e32 v104, 0, v62
	v_max_f32_e32 v105, 0, v63
	v_pk_add_f32 v[104:105], v[104:105], v[106:107]
	v_cmp_lt_i32_e32 vcc, 16, v184
	v_cmp_lt_i32_e64 s[4:5], 17, v184
	v_pk_add_f32 v[106:107], v[62:63], v[104:105] neg_lo:[0,1] neg_hi:[0,1]
	v_cndmask_b32_e32 v104, 0, v104, vcc
	v_cndmask_b32_e64 v105, 0, v105, s[4:5]
	v_cndmask_b32_e32 v140, v161, v106, vcc
	v_cndmask_b32_e64 v141, v161, v107, s[4:5]
	v_and_b32_e32 v107, 0xffff0000, v105
	v_and_b32_e32 v106, 0xffff0000, v104
	v_pk_add_f32 v[102:103], v[104:105], v[102:103]
	v_or_b32_sdwa v110, v107, v104 dst_sel:DWORD dst_unused:UNUSED_PAD src0_sel:DWORD src1_sel:WORD_1
	v_pk_add_f32 v[104:105], v[104:105], v[106:107] neg_lo:[0,1] neg_hi:[0,1]
	v_add_f32_e32 v106, 1.0, v211
	v_add_f32_e32 v107, 1.0, v210
	v_log_f32_e32 v106, v106
	v_log_f32_e32 v107, v107
	v_cvt_pk_bf16_f32 v114, v104, v105
	v_max_f32_e32 v104, 0, v46
	v_max_f32_e32 v105, 0, v47
	v_pk_add_f32 v[104:105], v[104:105], v[106:107]
	v_cmp_lt_i32_e32 vcc, 48, v184
	v_cmp_lt_i32_e64 s[4:5], 49, v184
	v_pk_add_f32 v[106:107], v[46:47], v[104:105] neg_lo:[0,1] neg_hi:[0,1]
	v_cndmask_b32_e32 v104, 0, v104, vcc
	v_cndmask_b32_e64 v105, 0, v105, s[4:5]
	v_pk_add_f32 v[108:109], v[104:105], v[102:103]
	v_and_b32_e32 v103, 0xffff0000, v105
	v_and_b32_e32 v102, 0xffff0000, v104
	v_cndmask_b32_e32 v144, v161, v106, vcc
	v_or_b32_sdwa v106, v103, v104 dst_sel:DWORD dst_unused:UNUSED_PAD src0_sel:DWORD src1_sel:WORD_1
	v_pk_add_f32 v[102:103], v[104:105], v[102:103] neg_lo:[0,1] neg_hi:[0,1]
	v_add_f32_e32 v104, 1.0, v207
	v_add_f32_e32 v105, 1.0, v206
	v_log_f32_e32 v104, v104
	v_log_f32_e32 v105, v105
	v_max_f32_e32 v112, 0, v64
	v_max_f32_e32 v113, 0, v65
	v_cndmask_b32_e64 v145, v161, v107, s[4:5]
	v_pk_add_f32 v[104:105], v[112:113], v[104:105]
	v_cmp_lt_i32_e32 vcc, 18, v184
	v_cmp_lt_i32_e64 s[4:5], 19, v184
	v_pk_add_f32 v[112:113], v[64:65], v[104:105] neg_lo:[0,1] neg_hi:[0,1]
	v_cndmask_b32_e32 v104, 0, v104, vcc
	v_cndmask_b32_e64 v105, 0, v105, s[4:5]
	v_cvt_pk_bf16_f32 v102, v102, v103
	v_cndmask_b32_e32 v146, v161, v112, vcc
	v_cndmask_b32_e64 v147, v161, v113, s[4:5]
	v_and_b32_e32 v113, 0xffff0000, v105
	v_and_b32_e32 v112, 0xffff0000, v104
	v_add_f32_e32 v103, 1.0, v203
	v_pk_add_f32 v[108:109], v[104:105], v[108:109]
	v_or_b32_sdwa v111, v113, v104 dst_sel:DWORD dst_unused:UNUSED_PAD src0_sel:DWORD src1_sel:WORD_1
	v_pk_add_f32 v[104:105], v[104:105], v[112:113] neg_lo:[0,1] neg_hi:[0,1]
	v_log_f32_e32 v112, v103
	v_add_f32_e32 v103, 1.0, v202
	v_log_f32_e32 v113, v103
	v_cvt_pk_bf16_f32 v115, v104, v105
	v_max_f32_e32 v104, 0, v48
	v_max_f32_e32 v105, 0, v49
	v_pk_add_f32 v[104:105], v[104:105], v[112:113]
	v_cmp_lt_i32_e32 vcc, 50, v184
	v_cmp_lt_i32_e64 s[4:5], 51, v184
	v_pk_add_f32 v[112:113], v[48:49], v[104:105] neg_lo:[0,1] neg_hi:[0,1]
	v_cndmask_b32_e32 v104, 0, v104, vcc
	v_cndmask_b32_e64 v105, 0, v105, s[4:5]
	v_cndmask_b32_e32 v152, v161, v112, vcc
	v_cndmask_b32_e64 v153, v161, v113, s[4:5]
	v_and_b32_e32 v113, 0xffff0000, v105
	v_and_b32_e32 v112, 0xffff0000, v104
	v_add_f32_e32 v103, 1.0, v199
	v_pk_add_f32 v[108:109], v[104:105], v[108:109]
	v_or_b32_sdwa v107, v113, v104 dst_sel:DWORD dst_unused:UNUSED_PAD src0_sel:DWORD src1_sel:WORD_1
	v_pk_add_f32 v[104:105], v[104:105], v[112:113] neg_lo:[0,1] neg_hi:[0,1]
	v_log_f32_e32 v112, v103
	v_add_f32_e32 v103, 1.0, v198
	v_log_f32_e32 v113, v103
	v_cvt_pk_bf16_f32 v103, v104, v105
	v_max_f32_e32 v104, 0, v66
	v_max_f32_e32 v105, 0, v67
	v_pk_add_f32 v[104:105], v[104:105], v[112:113]
	v_cmp_lt_i32_e64 s[4:5], 25, v184
	v_pk_add_f32 v[112:113], v[66:67], v[104:105] neg_lo:[0,1] neg_hi:[0,1]
	v_cmp_lt_i32_e32 vcc, 24, v184
	v_cndmask_b32_e64 v157, v161, v113, s[4:5]
	v_add_f32_e32 v113, 1.0, v195
	v_log_f32_e32 v142, v113
	v_add_f32_e32 v113, 1.0, v194
	v_cndmask_b32_e64 v105, 0, v105, s[4:5]
	v_cndmask_b32_e32 v104, 0, v104, vcc
	v_log_f32_e32 v143, v113
	v_and_b32_e32 v117, 0xffff0000, v105
	v_and_b32_e32 v116, 0xffff0000, v104
	v_cndmask_b32_e32 v156, v161, v112, vcc
	v_pk_add_f32 v[108:109], v[104:105], v[108:109]
	v_or_b32_sdwa v112, v117, v104 dst_sel:DWORD dst_unused:UNUSED_PAD src0_sel:DWORD src1_sel:WORD_1
	v_pk_add_f32 v[104:105], v[104:105], v[116:117] neg_lo:[0,1] neg_hi:[0,1]
	v_cmp_lt_i32_e32 vcc, 56, v184
	v_cvt_pk_bf16_f32 v116, v104, v105
	v_max_f32_e32 v104, 0, v50
	v_max_f32_e32 v105, 0, v51
	v_pk_add_f32 v[104:105], v[104:105], v[142:143]
	v_cmp_lt_i32_e64 s[4:5], 57, v184
	v_pk_add_f32 v[142:143], v[50:51], v[104:105] neg_lo:[0,1] neg_hi:[0,1]
	v_cndmask_b32_e32 v104, 0, v104, vcc
	v_cndmask_b32_e64 v105, 0, v105, s[4:5]
	v_cndmask_b32_e32 v158, v161, v142, vcc
	v_cndmask_b32_e64 v159, v161, v143, s[4:5]
	v_pk_add_f32 v[142:143], v[104:105], v[108:109]
	v_and_b32_e32 v149, 0xffff0000, v105
	v_and_b32_e32 v148, 0xffff0000, v104
	v_add_f32_e32 v109, 1.0, v190
	v_or_b32_sdwa v108, v149, v104 dst_sel:DWORD dst_unused:UNUSED_PAD src0_sel:DWORD src1_sel:WORD_1
	v_pk_add_f32 v[104:105], v[104:105], v[148:149] neg_lo:[0,1] neg_hi:[0,1]
	v_log_f32_e32 v148, v109
	v_add_f32_e32 v109, 1.0, v189
	v_log_f32_e32 v149, v109
	v_max_f32_e32 v150, 0, v68
	v_max_f32_e32 v151, 0, v69
	v_cmp_lt_i32_e32 vcc, 26, v184
	v_pk_add_f32 v[148:149], v[150:151], v[148:149]
	v_cmp_lt_i32_e64 s[4:5], 27, v184
	v_pk_add_f32 v[150:151], v[68:69], v[148:149] neg_lo:[0,1] neg_hi:[0,1]
	v_cndmask_b32_e32 v148, 0, v148, vcc
	v_cndmask_b32_e64 v149, 0, v149, s[4:5]
	v_cvt_pk_bf16_f32 v104, v104, v105
	v_cndmask_b32_e32 v154, v161, v150, vcc
	v_cndmask_b32_e64 v155, v161, v151, s[4:5]
	v_and_b32_e32 v151, 0xffff0000, v149
	v_and_b32_e32 v150, 0xffff0000, v148
	v_add_f32_e32 v105, 1.0, v187
	v_pk_add_f32 v[142:143], v[148:149], v[142:143]
	v_or_b32_sdwa v113, v151, v148 dst_sel:DWORD dst_unused:UNUSED_PAD src0_sel:DWORD src1_sel:WORD_1
	v_pk_add_f32 v[148:149], v[148:149], v[150:151] neg_lo:[0,1] neg_hi:[0,1]
	v_log_f32_e32 v150, v105
	v_add_f32_e32 v105, 1.0, v186
	v_log_f32_e32 v151, v105
	v_cvt_pk_bf16_f32 v117, v148, v149
	v_max_f32_e32 v148, 0, v52
	v_max_f32_e32 v149, 0, v53
	v_pk_add_f32 v[148:149], v[148:149], v[150:151]
	v_cmp_lt_i32_e32 vcc, 58, v184
	v_pk_add_f32 v[150:151], v[52:53], v[148:149] neg_lo:[0,1] neg_hi:[0,1]
	v_cmp_lt_i32_e64 s[4:5], 59, v184
	v_cndmask_b32_e32 v150, v161, v150, vcc
	v_cndmask_b32_e32 v148, 0, v148, vcc
	v_cndmask_b32_e64 v151, v161, v151, s[4:5]
	v_cndmask_b32_e64 v149, 0, v149, s[4:5]
	s_mov_b64 s[4:5], 0
.LBB0_542:
	s_andn2_b64 vcc, exec, s[4:5]
	s_cbranch_vccnz .LBB0_544
	v_add_f32_e32 v86, 1.0, v247
	v_add_f32_e32 v87, 1.0, v246
	v_log_f32_e32 v86, v86
	v_log_f32_e32 v87, v87
	v_max_f32_e32 v88, 0, v54
	v_max_f32_e32 v89, 0, v55
	v_pk_add_f32 v[86:87], v[88:89], v[86:87]
	s_nop 0
	v_and_b32_e32 v89, 0xffff0000, v87
	v_and_b32_e32 v88, 0xffff0000, v86
	v_pk_add_f32 v[124:125], v[54:55], v[86:87] neg_lo:[0,1] neg_hi:[0,1]
	v_pk_add_f32 v[54:55], v[86:87], 0 op_sel_hi:[1,0]
	v_or_b32_sdwa v98, v89, v86 dst_sel:DWORD dst_unused:UNUSED_PAD src0_sel:DWORD src1_sel:WORD_1
	v_pk_add_f32 v[86:87], v[86:87], v[88:89] neg_lo:[0,1] neg_hi:[0,1]
	v_add_f32_e32 v88, 1.0, v243
	v_add_f32_e32 v89, 1.0, v242
	v_log_f32_e32 v88, v88
	v_log_f32_e32 v89, v89
	v_cvt_pk_bf16_f32 v94, v86, v87
	v_max_f32_e32 v86, 0, v38
	v_max_f32_e32 v87, 0, v39
	v_pk_add_f32 v[88:89], v[86:87], v[88:89]
	v_add_f32_e32 v87, 1.0, v239
	v_pk_add_f32 v[126:127], v[38:39], v[88:89] neg_lo:[0,1] neg_hi:[0,1]
	v_pk_add_f32 v[38:39], v[88:89], v[54:55]
	v_and_b32_e32 v55, 0xffff0000, v89
	v_and_b32_e32 v54, 0xffff0000, v88
	v_or_b32_sdwa v86, v55, v88 dst_sel:DWORD dst_unused:UNUSED_PAD src0_sel:DWORD src1_sel:WORD_1
	v_pk_add_f32 v[54:55], v[88:89], v[54:55] neg_lo:[0,1] neg_hi:[0,1]
	v_log_f32_e32 v88, v87
	v_add_f32_e32 v87, 1.0, v238
	v_log_f32_e32 v89, v87
	v_cvt_pk_bf16_f32 v90, v54, v55
	v_max_f32_e32 v54, 0, v56
	v_max_f32_e32 v55, 0, v57
	v_pk_add_f32 v[54:55], v[54:55], v[88:89]
	s_nop 0
	v_pk_add_f32 v[128:129], v[56:57], v[54:55] neg_lo:[0,1] neg_hi:[0,1]
	v_and_b32_e32 v57, 0xffff0000, v55
	v_and_b32_e32 v56, 0xffff0000, v54
	v_pk_add_f32 v[38:39], v[54:55], v[38:39]
	v_or_b32_sdwa v99, v57, v54 dst_sel:DWORD dst_unused:UNUSED_PAD src0_sel:DWORD src1_sel:WORD_1
	v_pk_add_f32 v[54:55], v[54:55], v[56:57] neg_lo:[0,1] neg_hi:[0,1]
	v_add_f32_e32 v56, 1.0, v235
	v_add_f32_e32 v57, 1.0, v234
	v_log_f32_e32 v56, v56
	v_log_f32_e32 v57, v57
	v_cvt_pk_bf16_f32 v95, v54, v55
	v_max_f32_e32 v54, 0, v40
	v_max_f32_e32 v55, 0, v41
	v_pk_add_f32 v[54:55], v[54:55], v[56:57]
	s_nop 0
	v_pk_add_f32 v[130:131], v[40:41], v[54:55] neg_lo:[0,1] neg_hi:[0,1]
	v_and_b32_e32 v41, 0xffff0000, v55
	v_and_b32_e32 v40, 0xffff0000, v54
	v_pk_add_f32 v[38:39], v[54:55], v[38:39]
	v_or_b32_sdwa v87, v41, v54 dst_sel:DWORD dst_unused:UNUSED_PAD src0_sel:DWORD src1_sel:WORD_1
	v_pk_add_f32 v[40:41], v[54:55], v[40:41] neg_lo:[0,1] neg_hi:[0,1]
	v_add_f32_e32 v54, 1.0, v231
	v_add_f32_e32 v55, 1.0, v230
	v_log_f32_e32 v54, v54
	v_log_f32_e32 v55, v55
	v_cvt_pk_bf16_f32 v91, v40, v41
	v_max_f32_e32 v40, 0, v58
	v_max_f32_e32 v41, 0, v59
	v_pk_add_f32 v[40:41], v[40:41], v[54:55]
	s_nop 0
	v_and_b32_e32 v55, 0xffff0000, v41
	v_and_b32_e32 v54, 0xffff0000, v40
	v_pk_add_f32 v[132:133], v[58:59], v[40:41] neg_lo:[0,1] neg_hi:[0,1]
	v_pk_add_f32 v[38:39], v[40:41], v[38:39]
	v_or_b32_sdwa v100, v55, v40 dst_sel:DWORD dst_unused:UNUSED_PAD src0_sel:DWORD src1_sel:WORD_1
	v_pk_add_f32 v[40:41], v[40:41], v[54:55] neg_lo:[0,1] neg_hi:[0,1]
	v_add_f32_e32 v54, 1.0, v227
	v_add_f32_e32 v55, 1.0, v226
	v_log_f32_e32 v54, v54
	v_log_f32_e32 v55, v55
	v_cvt_pk_bf16_f32 v96, v40, v41
	v_max_f32_e32 v40, 0, v42
	v_max_f32_e32 v41, 0, v43
	v_pk_add_f32 v[40:41], v[40:41], v[54:55]
	v_max_f32_e32 v58, 0, v46
	v_pk_add_f32 v[134:135], v[42:43], v[40:41] neg_lo:[0,1] neg_hi:[0,1]
	v_and_b32_e32 v43, 0xffff0000, v41
	v_and_b32_e32 v42, 0xffff0000, v40
	v_pk_add_f32 v[38:39], v[40:41], v[38:39]
	v_or_b32_sdwa v88, v43, v40 dst_sel:DWORD dst_unused:UNUSED_PAD src0_sel:DWORD src1_sel:WORD_1
	v_pk_add_f32 v[40:41], v[40:41], v[42:43] neg_lo:[0,1] neg_hi:[0,1]
	v_add_f32_e32 v42, 1.0, v223
	v_log_f32_e32 v43, v42
	v_add_f32_e32 v42, 1.0, v222
	v_log_f32_e32 v42, v42
	v_cvt_pk_bf16_f32 v92, v40, v41
	v_max_f32_e32 v41, 0, v60
	v_max_f32_e32 v40, 0, v61
	v_pk_add_f32 v[40:41], v[40:41], v[42:43]
	v_max_f32_e32 v59, 0, v47
	v_and_b32_e32 v43, 0xffff0000, v40
	v_and_b32_e32 v42, 0xffff0000, v41
	v_pk_add_f32 v[136:137], v[60:61], v[40:41] op_sel:[0,1] op_sel_hi:[1,0] neg_lo:[0,1] neg_hi:[0,1]
	v_pk_add_f32 v[38:39], v[40:41], v[38:39] op_sel:[1,0] op_sel_hi:[0,1]
	v_or_b32_sdwa v101, v43, v41 dst_sel:DWORD dst_unused:UNUSED_PAD src0_sel:DWORD src1_sel:WORD_1
	v_pk_add_f32 v[40:41], v[40:41], v[42:43] op_sel:[1,0] op_sel_hi:[0,1] neg_lo:[0,1] neg_hi:[0,1]
	v_add_f32_e32 v42, 1.0, v219
	v_log_f32_e32 v43, v42
	v_add_f32_e32 v42, 1.0, v218
	v_log_f32_e32 v42, v42
	v_cvt_pk_bf16_f32 v97, v40, v41
	v_max_f32_e32 v41, 0, v44
	v_max_f32_e32 v40, 0, v45
	v_pk_add_f32 v[40:41], v[40:41], v[42:43]
	s_nop 0
	v_and_b32_e32 v43, 0xffff0000, v40
	v_and_b32_e32 v42, 0xffff0000, v41
	v_pk_add_f32 v[138:139], v[44:45], v[40:41] op_sel:[0,1] op_sel_hi:[1,0] neg_lo:[0,1] neg_hi:[0,1]
	v_pk_add_f32 v[38:39], v[40:41], v[38:39] op_sel:[1,0] op_sel_hi:[0,1]
	v_or_b32_sdwa v89, v43, v41 dst_sel:DWORD dst_unused:UNUSED_PAD src0_sel:DWORD src1_sel:WORD_1
	v_pk_add_f32 v[40:41], v[40:41], v[42:43] op_sel:[1,0] op_sel_hi:[0,1] neg_lo:[0,1] neg_hi:[0,1]
	v_add_f32_e32 v43, 1.0, v211
	v_cvt_pk_bf16_f32 v93, v40, v41
	v_add_f32_e32 v41, 1.0, v215
	v_log_f32_e32 v54, v43
	v_add_f32_e32 v43, 1.0, v210
	v_log_f32_e32 v42, v41
	v_add_f32_e32 v41, 1.0, v213
	v_log_f32_e32 v55, v43
	v_log_f32_e32 v56, v41
	v_add_f32_e32 v41, 1.0, v207
	v_add_f32_e32 v43, 1.0, v206
	v_log_f32_e32 v43, v43
	v_log_f32_e32 v57, v41
	v_pk_add_f32 v[54:55], v[58:59], v[54:55]
	v_max_f32_e32 v40, 0, v62
	v_max_f32_e32 v44, 0, v63
	v_pk_add_f32 v[144:145], v[46:47], v[54:55] neg_lo:[0,1] neg_hi:[0,1]
	v_and_b32_e32 v47, 0xffff0000, v55
	v_and_b32_e32 v46, 0xffff0000, v54
	v_max_f32_e32 v45, 0, v64
	v_max_f32_e32 v41, 0, v65
	v_or_b32_sdwa v106, v47, v54 dst_sel:DWORD dst_unused:UNUSED_PAD src0_sel:DWORD src1_sel:WORD_1
	v_pk_add_f32 v[46:47], v[54:55], v[46:47] neg_lo:[0,1] neg_hi:[0,1]
	v_pk_add_f32 v[40:41], v[40:41], v[42:43]
	v_pk_add_f32 v[42:43], v[44:45], v[56:57]
	v_cvt_pk_bf16_f32 v102, v46, v47
	v_and_b32_e32 v47, 0xffff0000, v42
	v_and_b32_e32 v57, 0xffff0000, v41
	v_mov_b32_e32 v44, v40
	v_mov_b32_e32 v45, v42
	v_or_b32_sdwa v111, v57, v43 dst_sel:DWORD dst_unused:UNUSED_PAD src0_sel:DWORD src1_sel:WORD_1
	v_or_b32_sdwa v110, v40, v47 dst_sel:DWORD dst_unused:UNUSED_PAD src0_sel:WORD_1 src1_sel:DWORD
	v_and_b32_e32 v46, 0xffff0000, v40
	v_mov_b32_e32 v40, v43
	v_and_b32_e32 v56, 0xffff0000, v43
	v_add_f32_e32 v42, 1.0, v203
	v_add_f32_e32 v43, 1.0, v202
	v_pk_add_f32 v[38:39], v[44:45], v[38:39]
	v_log_f32_e32 v42, v42
	v_log_f32_e32 v43, v43
	v_pk_add_f32 v[38:39], v[54:55], v[38:39]
	v_pk_add_f32 v[146:147], v[64:65], v[40:41] neg_lo:[0,1] neg_hi:[0,1]
	v_pk_add_f32 v[38:39], v[40:41], v[38:39]
	v_pk_add_f32 v[40:41], v[40:41], v[56:57] neg_lo:[0,1] neg_hi:[0,1]
	v_pk_add_f32 v[140:141], v[62:63], v[44:45] neg_lo:[0,1] neg_hi:[0,1]
	v_cvt_pk_bf16_f32 v115, v40, v41
	v_max_f32_e32 v40, 0, v48
	v_max_f32_e32 v41, 0, v49
	v_pk_add_f32 v[40:41], v[40:41], v[42:43]
	v_pk_add_f32 v[44:45], v[44:45], v[46:47] neg_lo:[0,1] neg_hi:[0,1]
	v_and_b32_e32 v43, 0xffff0000, v41
	v_and_b32_e32 v42, 0xffff0000, v40
	v_pk_add_f32 v[152:153], v[48:49], v[40:41] neg_lo:[0,1] neg_hi:[0,1]
	v_pk_add_f32 v[38:39], v[40:41], v[38:39]
	v_or_b32_sdwa v107, v43, v40 dst_sel:DWORD dst_unused:UNUSED_PAD src0_sel:DWORD src1_sel:WORD_1
	v_pk_add_f32 v[40:41], v[40:41], v[42:43] neg_lo:[0,1] neg_hi:[0,1]
	v_add_f32_e32 v42, 1.0, v199
	v_add_f32_e32 v43, 1.0, v198
	v_log_f32_e32 v42, v42
	v_log_f32_e32 v43, v43
	v_cvt_pk_bf16_f32 v103, v40, v41
	v_max_f32_e32 v40, 0, v66
	v_max_f32_e32 v41, 0, v67
	v_pk_add_f32 v[40:41], v[40:41], v[42:43]
	v_cvt_pk_bf16_f32 v114, v44, v45
	v_and_b32_e32 v43, 0xffff0000, v41
	v_and_b32_e32 v42, 0xffff0000, v40
	v_pk_add_f32 v[156:157], v[66:67], v[40:41] neg_lo:[0,1] neg_hi:[0,1]
	v_pk_add_f32 v[38:39], v[40:41], v[38:39]
	v_or_b32_sdwa v112, v43, v40 dst_sel:DWORD dst_unused:UNUSED_PAD src0_sel:DWORD src1_sel:WORD_1
	v_pk_add_f32 v[40:41], v[40:41], v[42:43] neg_lo:[0,1] neg_hi:[0,1]
	v_add_f32_e32 v42, 1.0, v195
	v_log_f32_e32 v43, v42
	v_add_f32_e32 v42, 1.0, v194
	v_log_f32_e32 v42, v42
	v_cvt_pk_bf16_f32 v116, v40, v41
	v_max_f32_e32 v41, 0, v50
	v_max_f32_e32 v40, 0, v51
	v_pk_add_f32 v[40:41], v[40:41], v[42:43]
	s_nop 0
	v_and_b32_e32 v43, 0xffff0000, v40
	v_and_b32_e32 v42, 0xffff0000, v41
	v_pk_add_f32 v[158:159], v[50:51], v[40:41] op_sel:[0,1] op_sel_hi:[1,0] neg_lo:[0,1] neg_hi:[0,1]
	v_pk_add_f32 v[38:39], v[40:41], v[38:39] op_sel:[1,0] op_sel_hi:[0,1]
	v_or_b32_sdwa v108, v43, v41 dst_sel:DWORD dst_unused:UNUSED_PAD src0_sel:DWORD src1_sel:WORD_1
	v_pk_add_f32 v[40:41], v[40:41], v[42:43] op_sel:[1,0] op_sel_hi:[0,1] neg_lo:[0,1] neg_hi:[0,1]
	v_add_f32_e32 v42, 1.0, v190
	v_log_f32_e32 v43, v42
	v_add_f32_e32 v42, 1.0, v189
	v_log_f32_e32 v42, v42
	v_cvt_pk_bf16_f32 v104, v40, v41
	v_max_f32_e32 v41, 0, v68
	v_max_f32_e32 v40, 0, v69
	v_pk_add_f32 v[40:41], v[40:41], v[42:43]
	s_nop 0
	v_pk_add_f32 v[142:143], v[40:41], v[38:39] op_sel:[1,0] op_sel_hi:[0,1]
	v_and_b32_e32 v39, 0xffff0000, v40
	v_and_b32_e32 v38, 0xffff0000, v41
	v_pk_add_f32 v[154:155], v[68:69], v[40:41] op_sel:[0,1] op_sel_hi:[1,0] neg_lo:[0,1] neg_hi:[0,1]
	v_or_b32_sdwa v113, v39, v41 dst_sel:DWORD dst_unused:UNUSED_PAD src0_sel:DWORD src1_sel:WORD_1
	v_pk_add_f32 v[38:39], v[40:41], v[38:39] op_sel:[1,0] op_sel_hi:[0,1] neg_lo:[0,1] neg_hi:[0,1]
	v_add_f32_e32 v40, 1.0, v187
	v_add_f32_e32 v41, 1.0, v186
	v_log_f32_e32 v40, v40
	v_log_f32_e32 v41, v41
	v_cvt_pk_bf16_f32 v117, v38, v39
	v_max_f32_e32 v38, 0, v52
	v_max_f32_e32 v39, 0, v53
	v_pk_add_f32 v[148:149], v[38:39], v[40:41]
	s_nop 0
	v_pk_add_f32 v[150:151], v[52:53], v[148:149] neg_lo:[0,1] neg_hi:[0,1]
.LBB0_544:
	s_mov_b32 s4, 0x43000000
	s_sub_i32 s18, s44, s17
	v_mov_b32_e32 v37, v36
	v_mov_b32_e32 v38, v36
	v_mov_b32_e32 v39, v36
	v_mov_b32_e32 v40, v36
	v_mov_b32_e32 v41, v36
	v_mov_b32_e32 v42, v36
	v_mov_b32_e32 v43, v36
	v_mov_b32_e32 v44, v36
	v_mov_b32_e32 v45, v36
	v_mov_b32_e32 v46, v36
	v_mov_b32_e32 v47, v36
	v_mov_b32_e32 v48, v36
	v_mov_b32_e32 v49, v36
	v_mov_b32_e32 v50, v36
	v_mov_b32_e32 v51, v36
	v_and_b32_e32 v53, 0xffff0000, v149
	v_and_b32_e32 v52, 0xffff0000, v148
	v_add_u32_e32 v3, s18, v167
	v_mfma_f32_32x32x16_bf16 v[54:69], v[172:175], v[98:101], v[36:51]
	v_or_b32_sdwa v109, v53, v148 dst_sel:DWORD dst_unused:UNUSED_PAD src0_sel:DWORD src1_sel:WORD_1
	v_add_f32_e64 v52, v148, -v52
	v_add_f32_e64 v53, v149, -v53
	v_mfma_f32_32x32x16_bf16 v[200:215], v[172:175], v[86:89], v[36:51]
	v_cvt_pk_bf16_f32 v105, v52, v53
	v_mfma_f32_32x32x16_bf16 v[54:69], v[172:175], v[94:97], v[54:69]
	v_mfma_f32_32x32x16_bf16 v[200:215], v[172:175], v[90:93], v[200:215]
	v_mfma_f32_32x32x16_bf16 v[54:69], v[176:179], v[110:113], v[54:69]
	v_mfma_f32_32x32x16_bf16 v[54:69], v[176:179], v[114:117], v[54:69]
	v_mfma_f32_32x32x16_bf16 v[54:69], v[180:183], v[86:89], v[54:69]
	v_mfma_f32_32x32x16_bf16 v[200:215], v[176:179], v[106:109], v[200:215]
	v_mfma_f32_32x32x16_bf16 v[54:69], v[180:183], v[90:93], v[54:69]
	v_mfma_f32_32x32x16_bf16 v[54:69], v[180:183], v[106:109], v[54:69]
	v_mfma_f32_32x32x16_bf16 v[200:215], v[176:179], v[102:105], v[200:215]
	v_mfma_f32_32x32x16_bf16 v[54:69], v[180:183], v[102:105], v[54:69]
	s_nop 10
	v_sub_f32_e32 v38, v126, v200
	v_exp_f32_e32 v100, v38
	v_sub_f32_e32 v38, v125, v55
	v_exp_f32_e32 v55, v38
	v_sub_f32_e32 v38, v127, v201
	v_exp_f32_e32 v101, v38
	v_sub_f32_e32 v38, v128, v56
	v_exp_f32_e32 v56, v38
	v_sub_f32_e32 v38, v130, v202
	v_exp_f32_e32 v102, v38
	v_sub_f32_e32 v38, v129, v57
	v_exp_f32_e32 v57, v38
	v_sub_f32_e32 v38, v131, v203
	v_exp_f32_e32 v103, v38
	v_sub_f32_e32 v38, v132, v58
	v_exp_f32_e32 v58, v38
	v_sub_f32_e32 v38, v134, v204
	v_exp_f32_e32 v104, v38
	v_sub_f32_e32 v38, v133, v59
	v_exp_f32_e32 v59, v38
	v_sub_f32_e32 v38, v135, v205
	v_exp_f32_e32 v105, v38
	v_sub_f32_e32 v38, v136, v60
	v_exp_f32_e32 v60, v38
	v_sub_f32_e32 v38, v138, v206
	v_exp_f32_e32 v106, v38
	v_sub_f32_e32 v38, v137, v61
	v_exp_f32_e32 v61, v38
	v_sub_f32_e32 v38, v139, v207
	v_exp_f32_e32 v107, v38
	v_sub_f32_e32 v38, v140, v62
	v_exp_f32_e32 v62, v38
	v_sub_f32_e32 v38, v144, v208
	v_exp_f32_e32 v108, v38
	v_sub_f32_e32 v38, v141, v63
	v_exp_f32_e32 v63, v38
	v_sub_f32_e32 v38, v145, v209
	v_exp_f32_e32 v109, v38
	v_sub_f32_e32 v38, v146, v64
	v_exp_f32_e32 v64, v38
	v_sub_f32_e32 v38, v152, v210
	v_exp_f32_e32 v110, v38
	v_sub_f32_e32 v38, v147, v65
	v_exp_f32_e32 v65, v38
	v_sub_f32_e32 v38, v153, v211
	v_exp_f32_e32 v111, v38
	v_sub_f32_e32 v38, v156, v66
	v_exp_f32_e32 v66, v38
	v_sub_f32_e32 v38, v158, v212
	v_exp_f32_e32 v112, v38
	v_sub_f32_e32 v38, v157, v67
	v_exp_f32_e32 v50, v38
	v_sub_f32_e32 v38, v159, v213
	v_exp_f32_e32 v67, v38
	v_sub_f32_e32 v38, v154, v68
	v_sub_f32_e32 v54, v124, v54
	v_exp_f32_e32 v51, v38
	v_exp_f32_e32 v54, v54
	ds_read_b64_tr_b16 v[38:39], v3
	ds_read_b64_tr_b16 v[40:41], v3 offset:512
	ds_read_b64_tr_b16 v[48:49], v3 offset:4608
	ds_read_b64_tr_b16 v[46:47], v3 offset:4096
	v_cvt_pk_bf16_f32 v43, v56, v57
	v_cvt_pk_bf16_f32 v42, v54, v55
	v_cvt_pk_bf16_f32 v44, v58, v59
	v_cvt_pk_bf16_f32 v45, v60, v61
	s_waitcnt lgkmcnt(2)
	s_nop 0
	v_mfma_f32_32x32x16_bf16 v[20:35], v[38:41], v[42:45], v[20:35]
	v_sub_f32_e32 v38, v155, v69
	v_exp_f32_e32 v41, v38
	ds_read_b64_tr_b16 v[54:55], v3 offset:1024
	ds_read_b64_tr_b16 v[56:57], v3 offset:1536
	v_cvt_pk_bf16_f32 v38, v62, v63
	v_cvt_pk_bf16_f32 v39, v64, v65
	s_waitcnt lgkmcnt(2)
	v_mfma_f32_32x32x16_bf16 v[4:19], v[46:49], v[42:45], v[4:19]
	ds_read_b64_tr_b16 v[42:43], v3 offset:5120
	ds_read_b64_tr_b16 v[44:45], v3 offset:5632
	v_cvt_pk_bf16_f32 v40, v66, v50
	v_cvt_pk_bf16_f32 v41, v51, v41
	s_waitcnt lgkmcnt(2)
	v_mfma_f32_32x32x16_bf16 v[20:35], v[54:57], v[38:41], v[20:35]
	ds_read_b64_tr_b16 v[54:55], v3 offset:2048
	ds_read_b64_tr_b16 v[56:57], v3 offset:2560
	v_sub_f32_e32 v46, v150, v214
	v_exp_f32_e32 v58, v46
	v_cvt_pk_bf16_f32 v46, v100, v101
	v_cvt_pk_bf16_f32 v47, v102, v103
	v_cvt_pk_bf16_f32 v48, v104, v105
	v_cvt_pk_bf16_f32 v49, v106, v107
	s_waitcnt lgkmcnt(2)
	v_mfma_f32_32x32x16_bf16 v[4:19], v[42:45], v[38:41], v[4:19]
	ds_read_b64_tr_b16 v[38:39], v3 offset:6144
	ds_read_b64_tr_b16 v[40:41], v3 offset:6656
	v_sub_f32_e32 v42, v151, v215
	v_exp_f32_e32 v45, v42
	s_waitcnt lgkmcnt(2)
	v_mfma_f32_32x32x16_bf16 v[20:35], v[54:57], v[46:49], v[20:35]
	ds_read_b64_tr_b16 v[50:51], v3 offset:3072
	ds_read_b64_tr_b16 v[52:53], v3 offset:3584
	v_cvt_pk_bf16_f32 v42, v108, v109
	v_cvt_pk_bf16_f32 v43, v110, v111
	v_cvt_pk_bf16_f32 v44, v112, v67
	v_cvt_pk_bf16_f32 v45, v58, v45
	s_waitcnt lgkmcnt(2)
	v_mfma_f32_32x32x16_bf16 v[4:19], v[38:41], v[46:49], v[4:19]
	ds_read_b64_tr_b16 v[38:39], v3 offset:7168
	ds_read_b64_tr_b16 v[40:41], v3 offset:7680
	v_add_f32_e64 v46, v148, v142
	v_add_f32_e64 v47, v149, v143
	v_pk_add_f32 v[46:47], v[46:47], v[46:47] op_sel:[0,1] op_sel_hi:[1,0]
	s_nop 0
	v_mov_b32_e32 v3, v46
	s_nop 1
	v_permlane32_swap_b32_e32 v46, v3
	s_waitcnt lgkmcnt(2)
	v_mfma_f32_32x32x16_bf16 v[20:35], v[50:53], v[42:45], v[20:35]
	v_add_f32_e32 v3, v46, v3
	v_add_f32_e32 v36, v36, v3
	v_cmp_lt_f32_e32 vcc, s4, v36
	s_cmp_eq_u64 vcc, exec
	s_cselect_b64 s[4:5], -1, 0
	s_waitcnt lgkmcnt(0)
	v_mfma_f32_32x32x16_bf16 v[4:19], v[38:41], v[42:45], v[4:19]
